# speedup vs baseline: 1.0150x; 1.0150x over previous
.LBB1_8:
	s_or_b64 exec, exec, s[4:5]
	v_add_u32_e32 v10, v172, v2
	s_waitcnt lgkmcnt(0)
	s_barrier
	ds_read_b128 v[18:21], v10 offset:256
	ds_read_b128 v[22:25], v10 offset:288
	ds_read_b128 v[82:85], v10 offset:320
	ds_read_b128 v[86:89], v10 offset:352
	ds_read_b128 v[74:77], v10 offset:384
	ds_read_b128 v[78:81], v10 offset:416
	ds_read_b128 v[2:5], v213 offset:32768
	ds_read_b128 v[6:9], v213 offset:0
	ds_read_b128 v[66:69], v10 offset:448
	ds_read_b128 v[70:73], v10 offset:480
	ds_read_b128 v[10:13], v213 offset:1024
	s_waitcnt lgkmcnt(3)
	v_pk_mul_f32 v[26:27], v[8:9], v[20:21]
	v_pk_mul_f32 v[28:29], v[6:7], v[18:19]
	ds_read_b128 v[14:17], v213 offset:8192
	s_waitcnt lgkmcnt(1)
	v_pk_mul_f32 v[12:13], v[12:13], v[24:25]
	v_pk_mul_f32 v[10:11], v[10:11], v[22:23]
	v_pk_fma_f32 v[30:31], v[8:9], v[20:21], v[12:13]
	v_pk_fma_f32 v[32:33], v[6:7], v[18:19], v[10:11]
	v_cvt_pk_bf16_f32 v9, v12, v13
	v_cvt_pk_bf16_f32 v7, v26, v27
	v_cvt_pk_bf16_f32 v8, v10, v11
	v_cvt_pk_bf16_f32 v6, v28, v29
	ds_read_b128 v[10:13], v213 offset:33792
	s_nop 0
	v_mfma_f32_32x32x16_bf16 v[34:49], v[2:5], v[6:9], 0
	ds_read_b128 v[6:9], v213 offset:9216
	s_waitcnt lgkmcnt(2)
	v_mul_f32_e32 v26, v16, v20
	v_mul_f32_e32 v27, v17, v21
	v_pk_mul_f32 v[50:51], v[14:15], v[18:19]
	s_mov_b32 s4, 0x3727c5ac
	s_waitcnt lgkmcnt(0)
	v_pk_mul_f32 v[8:9], v[8:9], v[24:25]
	v_pk_mul_f32 v[28:29], v[6:7], v[22:23]
	v_pk_fma_f32 v[90:91], v[16:17], v[20:21], v[8:9]
	v_pk_fma_f32 v[92:93], v[14:15], v[18:19], v[28:29]
	ds_read_b128 v[14:17], v213 offset:2048
	v_cvt_pk_bf16_f32 v9, v8, v9
	v_cvt_pk_bf16_f32 v7, v26, v27
	v_cvt_pk_bf16_f32 v8, v28, v29
	ds_read_b128 v[26:29], v213 offset:3072
	v_cvt_pk_bf16_f32 v6, v50, v51
	s_waitcnt lgkmcnt(1)
	v_pk_mul_f32 v[94:95], v[14:15], v[82:83]
	s_mov_b32 s0, 0x3c800000
	v_mfma_f32_32x32x16_bf16 v[50:65], v[2:5], v[6:9], 0
	v_mul_f32_e32 v2, v16, v84
	v_mul_f32_e32 v3, v17, v85
	s_waitcnt lgkmcnt(0)
	v_mul_f32_e32 v4, v28, v88
	v_mul_f32_e32 v5, v29, v89
	v_pk_mul_f32 v[6:7], v[26:27], v[86:87]
	v_pk_fma_f32 v[8:9], v[16:17], v[84:85], v[4:5]
	v_cvt_pk_bf16_f32 v3, v2, v3
	v_pk_fma_f32 v[14:15], v[14:15], v[82:83], v[6:7]
	v_pk_add_f32 v[26:27], v[8:9], v[30:31]
	v_cvt_pk_bf16_f32 v5, v4, v5
	v_cvt_pk_bf16_f32 v4, v6, v7
	ds_read_b128 v[6:9], v213 offset:10240
	v_pk_add_f32 v[28:29], v[14:15], v[32:33]
	ds_read_b128 v[14:17], v213 offset:11264
	v_cvt_pk_bf16_f32 v2, v94, v95
	s_waitcnt lgkmcnt(1)
	v_pk_mul_f32 v[30:31], v[6:7], v[82:83]
	v_mov_b64_e32 v[152:153], s[4:5]
	v_mfma_f32_32x32x16_bf16 v[34:49], v[10:13], v[2:5], v[34:49]
	v_mul_f32_e32 v2, v8, v84
	v_mul_f32_e32 v3, v9, v85
	s_waitcnt lgkmcnt(0)
	v_mul_f32_e32 v4, v16, v88
	v_mul_f32_e32 v5, v17, v89
	v_pk_mul_f32 v[14:15], v[14:15], v[86:87]
	v_pk_fma_f32 v[8:9], v[8:9], v[84:85], v[4:5]
	v_pk_fma_f32 v[6:7], v[6:7], v[82:83], v[14:15]
	v_cvt_pk_bf16_f32 v5, v4, v5
	v_cvt_pk_bf16_f32 v3, v2, v3
	v_cvt_pk_bf16_f32 v4, v14, v15
	v_pk_add_f32 v[32:33], v[8:9], v[90:91]
	v_pk_add_f32 v[90:91], v[6:7], v[92:93]
	ds_read_b128 v[6:9], v213 offset:34816
	ds_read_b128 v[14:17], v213 offset:4096
	v_cvt_pk_bf16_f32 v2, v30, v31
	s_mov_b32 s13, 0
	s_mov_b64 s[6:7], 0
	v_mfma_f32_32x32x16_bf16 v[50:65], v[10:13], v[2:5], v[50:65]
	ds_read_b128 v[2:5], v213 offset:5120
	ds_read_b128 v[10:13], v213 offset:12288
	s_waitcnt lgkmcnt(2)
	v_pk_mul_f32 v[30:31], v[16:17], v[76:77]
	v_pk_mul_f32 v[92:93], v[14:15], v[74:75]
	s_waitcnt lgkmcnt(1)
	v_pk_mul_f32 v[4:5], v[4:5], v[80:81]
	v_pk_mul_f32 v[94:95], v[2:3], v[78:79]
	v_pk_fma_f32 v[2:3], v[16:17], v[76:77], v[4:5]
	v_cvt_pk_bf16_f32 v5, v4, v5
	v_pk_add_f32 v[96:97], v[2:3], v[26:27]
	v_cvt_pk_bf16_f32 v3, v30, v31
	v_cvt_pk_bf16_f32 v4, v94, v95
	v_cvt_pk_bf16_f32 v2, v92, v93
	v_pk_fma_f32 v[14:15], v[14:15], v[74:75], v[94:95]
	s_waitcnt lgkmcnt(0)
	v_pk_mul_f32 v[30:31], v[10:11], v[74:75]
	v_mfma_f32_32x32x16_bf16 v[34:49], v[6:9], v[2:5], v[34:49]
	ds_read_b128 v[2:5], v213 offset:13312
	v_add_f32_e32 v98, v14, v28
	v_add_f32_e32 v99, v15, v29
	ds_read_b128 v[14:17], v213 offset:35840
	v_pk_mul_f32 v[26:27], v[12:13], v[76:77]
	s_waitcnt lgkmcnt(1)
	v_pk_mul_f32 v[4:5], v[4:5], v[80:81]
	v_pk_mul_f32 v[28:29], v[2:3], v[78:79]
	v_pk_fma_f32 v[2:3], v[12:13], v[76:77], v[4:5]
	v_pk_fma_f32 v[10:11], v[10:11], v[74:75], v[28:29]
	v_pk_add_f32 v[32:33], v[2:3], v[32:33]
	v_pk_add_f32 v[92:93], v[10:11], v[90:91]
	ds_read_b128 v[10:13], v213 offset:6144
	v_cvt_pk_bf16_f32 v5, v4, v5
	v_cvt_pk_bf16_f32 v3, v26, v27
	v_cvt_pk_bf16_f32 v4, v28, v29
	ds_read_b128 v[26:29], v213 offset:7168
	v_cvt_pk_bf16_f32 v2, v30, v31
	s_waitcnt lgkmcnt(1)
	v_pk_mul_f32 v[30:31], v[10:11], v[66:67]
	v_mfma_f32_32x32x16_bf16 v[50:65], v[6:9], v[2:5], v[50:65]
	v_mul_f32_e32 v2, v12, v68
	v_mul_f32_e32 v3, v13, v69
	s_waitcnt lgkmcnt(0)
	v_mul_f32_e32 v4, v28, v72
	v_mul_f32_e32 v5, v29, v73
	v_pk_mul_f32 v[6:7], v[26:27], v[70:71]
	v_pk_fma_f32 v[8:9], v[12:13], v[68:69], v[4:5]
	v_cvt_pk_bf16_f32 v3, v2, v3
	v_pk_fma_f32 v[10:11], v[10:11], v[66:67], v[6:7]
	v_pk_add_f32 v[94:95], v[8:9], v[96:97]
	v_cvt_pk_bf16_f32 v5, v4, v5
	v_cvt_pk_bf16_f32 v4, v6, v7
	ds_read_b128 v[6:9], v213 offset:14336
	v_pk_add_f32 v[96:97], v[10:11], v[98:99]
	ds_read_b128 v[10:13], v213 offset:15360
	v_cvt_pk_bf16_f32 v2, v30, v31
	s_waitcnt lgkmcnt(1)
	v_pk_mul_f32 v[30:31], v[6:7], v[66:67]
	v_mfma_f32_32x32x16_bf16 v[34:49], v[14:17], v[2:5], v[34:49]
	s_waitcnt lgkmcnt(0)
	v_mul_f32_e32 v10, v10, v70
	v_mul_f32_e32 v11, v11, v71
	v_mul_f32_e32 v2, v8, v68
	v_mul_f32_e32 v3, v9, v69
	v_pk_mul_f32 v[4:5], v[12:13], v[72:73]
	v_pk_fma_f32 v[6:7], v[6:7], v[66:67], v[10:11]
	v_pk_fma_f32 v[8:9], v[8:9], v[68:69], v[4:5]
	v_pk_add_f32 v[92:93], v[6:7], v[92:93]
	v_cvt_pk_bf16_f32 v3, v2, v3
	v_pk_add_f32 v[90:91], v[8:9], v[32:33]
	v_cvt_pk_bf16_f32 v5, v4, v5
	v_cvt_pk_bf16_f32 v4, v10, v11
	ds_read_b128 v[26:29], v213 offset:36864
	ds_read_b128 v[6:9], v213 offset:16384
	v_cvt_pk_bf16_f32 v2, v30, v31
	ds_read_b128 v[98:101], v213 offset:25600
	ds_read_b128 v[102:105], v213 offset:37888
	v_mfma_f32_32x32x16_bf16 v[50:65], v[14:17], v[2:5], v[50:65]
	ds_read_b128 v[2:5], v213 offset:17408
	ds_read_b128 v[30:33], v213 offset:24576
	s_waitcnt lgkmcnt(4)
	v_pk_mul_f32 v[12:13], v[6:7], v[18:19]
	v_pk_mul_f32 v[10:11], v[8:9], v[20:21]
	s_waitcnt lgkmcnt(1)
	v_pk_mul_f32 v[14:15], v[2:3], v[22:23]
	v_pk_mul_f32 v[22:23], v[98:99], v[22:23]
	v_pk_fma_f32 v[112:113], v[6:7], v[18:19], v[14:15]
	s_waitcnt lgkmcnt(0)
	v_pk_mul_f32 v[114:115], v[30:31], v[18:19]
	v_pk_fma_f32 v[118:119], v[30:31], v[18:19], v[22:23]
	v_pk_mul_f32 v[4:5], v[4:5], v[24:25]
	v_pk_mul_f32 v[106:107], v[32:33], v[20:21]
	v_pk_mul_f32 v[24:25], v[100:101], v[24:25]
	ds_read_b128 v[98:101], v213 offset:18432
	v_cvt_pk_bf16_f32 v19, v106, v107
	ds_read_b128 v[106:109], v213 offset:19456
	v_pk_fma_f32 v[110:111], v[8:9], v[20:21], v[4:5]
	v_cvt_pk_bf16_f32 v5, v4, v5
	v_cvt_pk_bf16_f32 v3, v10, v11
	v_cvt_pk_bf16_f32 v4, v14, v15
	s_waitcnt lgkmcnt(0)
	v_pk_mul_f32 v[106:107], v[106:107], v[86:87]
	v_cvt_pk_bf16_f32 v2, v12, v13
	v_pk_mul_f32 v[120:121], v[98:99], v[82:83]
	v_pk_mul_f32 v[108:109], v[108:109], v[88:89]
	v_pk_fma_f32 v[98:99], v[98:99], v[82:83], v[106:107]
	v_mfma_f32_32x32x16_bf16 v[2:17], v[26:29], v[2:5], 0
	v_cvt_pk_bf16_f32 v18, v114, v115
	v_mul_f32_e32 v114, v100, v84
	v_mul_f32_e32 v115, v101, v85
	v_fma_f32 v100, v100, v84, v108
	v_fma_f32 v101, v101, v85, v109
	v_pk_add_f32 v[124:125], v[98:99], v[112:113]
	v_pk_add_f32 v[122:123], v[100:101], v[110:111]
	v_cvt_pk_bf16_f32 v101, v108, v109
	v_cvt_pk_bf16_f32 v100, v106, v107
	ds_read_b128 v[106:109], v213 offset:26624
	v_pk_fma_f32 v[116:117], v[32:33], v[20:21], v[24:25]
	v_cvt_pk_bf16_f32 v21, v24, v25
	v_cvt_pk_bf16_f32 v20, v22, v23
	ds_read_b128 v[110:113], v213 offset:27648
	v_cvt_pk_bf16_f32 v99, v114, v115
	v_mfma_f32_32x32x16_bf16 v[18:33], v[26:29], v[18:21], 0
	v_cvt_pk_bf16_f32 v98, v120, v121
	s_waitcnt lgkmcnt(1)
	v_mul_f32_e32 v114, v106, v82
	v_mul_f32_e32 v115, v107, v83
	s_waitcnt lgkmcnt(0)
	v_pk_mul_f32 v[86:87], v[110:111], v[86:87]
	v_pk_mul_f32 v[88:89], v[112:113], v[88:89]
	v_pk_fma_f32 v[82:83], v[106:107], v[82:83], v[86:87]
	v_mfma_f32_32x32x16_bf16 v[2:17], v[102:105], v[98:101], v[2:17]
	v_mul_f32_e32 v98, v108, v84
	v_mul_f32_e32 v99, v109, v85
	v_fma_f32 v84, v108, v84, v88
	v_fma_f32 v85, v109, v85, v89
	v_add_f32_e32 v108, v82, v118
	v_add_f32_e32 v109, v83, v119
	v_cvt_pk_bf16_f32 v83, v98, v99
	v_pk_add_f32 v[106:107], v[84:85], v[116:117]
	v_cvt_pk_bf16_f32 v85, v88, v89
	v_cvt_pk_bf16_f32 v84, v86, v87
	ds_read_b128 v[86:89], v213 offset:38912
	ds_read_b128 v[98:101], v213 offset:20480
	v_cvt_pk_bf16_f32 v82, v114, v115
	s_waitcnt lgkmcnt(0)
	v_pk_mul_f32 v[110:111], v[100:101], v[76:77]
	v_mfma_f32_32x32x16_bf16 v[18:33], v[102:105], v[82:85], v[18:33]
	ds_read_b128 v[82:85], v213 offset:21504
	ds_read_b128 v[102:105], v213 offset:28672
	v_mul_f32_e32 v112, v98, v74
	v_mul_f32_e32 v113, v99, v75
	s_waitcnt lgkmcnt(1)
	v_pk_mul_f32 v[84:85], v[84:85], v[80:81]
	v_pk_mul_f32 v[114:115], v[82:83], v[78:79]
	v_pk_fma_f32 v[82:83], v[100:101], v[76:77], v[84:85]
	v_cvt_pk_bf16_f32 v85, v84, v85
	v_pk_add_f32 v[116:117], v[82:83], v[122:123]
	v_cvt_pk_bf16_f32 v83, v110, v111
	v_cvt_pk_bf16_f32 v84, v114, v115
	v_cvt_pk_bf16_f32 v82, v112, v113
	v_pk_fma_f32 v[98:99], v[98:99], v[74:75], v[114:115]
	s_waitcnt lgkmcnt(0)
	v_pk_mul_f32 v[112:113], v[102:103], v[74:75]
	v_mfma_f32_32x32x16_bf16 v[2:17], v[86:89], v[82:85], v[2:17]
	ds_read_b128 v[82:85], v213 offset:29696
	v_add_f32_e32 v118, v98, v124
	v_add_f32_e32 v119, v99, v125
	v_mul_f32_e32 v110, v104, v76
	v_mul_f32_e32 v111, v105, v77
	ds_read_b128 v[98:101], v213 offset:39936
	s_waitcnt lgkmcnt(1)
	v_pk_mul_f32 v[78:79], v[82:83], v[78:79]
	v_pk_mul_f32 v[80:81], v[84:85], v[80:81]
	v_pk_fma_f32 v[74:75], v[102:103], v[74:75], v[78:79]
	v_pk_fma_f32 v[76:77], v[104:105], v[76:77], v[80:81]
	v_pk_add_f32 v[104:105], v[74:75], v[108:109]
	v_pk_add_f32 v[102:103], v[76:77], v[106:107]
	v_cvt_pk_bf16_f32 v77, v80, v81
	v_cvt_pk_bf16_f32 v76, v78, v79
	ds_read_b128 v[78:81], v213 offset:22528
	ds_read_b128 v[82:85], v213 offset:23552
	v_cvt_pk_bf16_f32 v75, v110, v111
	v_cvt_pk_bf16_f32 v74, v112, v113
	s_waitcnt lgkmcnt(0)
	v_pk_mul_f32 v[82:83], v[82:83], v[70:71]
	v_mfma_f32_32x32x16_bf16 v[18:33], v[86:89], v[74:77], v[18:33]
	v_mul_f32_e32 v74, v80, v68
	v_mul_f32_e32 v75, v81, v69
	v_mul_f32_e32 v76, v84, v72
	v_mul_f32_e32 v77, v85, v73
	v_mul_f32_e32 v86, v78, v66
	v_mul_f32_e32 v87, v79, v67
	v_pk_fma_f32 v[80:81], v[80:81], v[68:69], v[76:77]
	v_pk_fma_f32 v[78:79], v[78:79], v[66:67], v[82:83]
	v_cvt_pk_bf16_f32 v75, v74, v75
	v_pk_add_f32 v[88:89], v[80:81], v[116:117]
	v_pk_add_f32 v[106:107], v[78:79], v[118:119]
	ds_read_b128 v[78:81], v213 offset:30720
	v_cvt_pk_bf16_f32 v77, v76, v77
	v_cvt_pk_bf16_f32 v76, v82, v83
	ds_read_b128 v[82:85], v213 offset:31744
	v_cvt_pk_bf16_f32 v74, v86, v87
	s_waitcnt lgkmcnt(0)
	v_pk_mul_f32 v[72:73], v[84:85], v[72:73]
	v_mfma_f32_32x32x16_bf16 v[2:17], v[98:101], v[74:77], v[2:17]
	v_mul_f32_e32 v74, v80, v68
	v_mul_f32_e32 v75, v81, v69
	v_fma_f32 v68, v80, v68, v72
	v_fma_f32 v69, v81, v69, v73
	v_mul_f32_e32 v70, v82, v70
	v_mul_f32_e32 v71, v83, v71
	v_pk_add_f32 v[84:85], v[68:69], v[102:103]
	v_cvt_pk_bf16_f32 v69, v72, v73
	v_pk_mov_b32 v[72:73], v[96:97], v[94:95] op_sel:[1,0]
	v_mov_b32_e32 v97, v95
	v_pk_add_f32 v[72:73], v[72:73], v[96:97]
	v_pk_mul_f32 v[76:77], v[78:79], v[66:67]
	v_pk_fma_f32 v[66:67], v[78:79], v[66:67], v[70:71]
	v_pk_add_f32 v[72:73], v[72:73], v[72:73] op_sel:[0,1] op_sel_hi:[1,0]
	v_pk_add_f32 v[86:87], v[66:67], v[104:105]
	v_mov_b32_e32 v66, v72
	s_nop 1
	v_permlane32_swap_b32_e32 v72, v66
	v_add_f32_e32 v66, v72, v66
	v_cvt_pk_bf16_f32 v67, v74, v75
	v_rcp_f32_e32 v74, v66
	v_cvt_pk_bf16_f32 v68, v70, v71
	v_cvt_pk_bf16_f32 v66, v76, v77
	v_pk_mul_f32 v[70:71], v[46:47], v[74:75] op_sel_hi:[1,0]
	s_nop 0
	v_mfma_f32_32x32x16_bf16 v[18:33], v[98:101], v[66:69], v[18:33]
	v_mul_f32_e32 v66, v42, v74
	v_mul_f32_e32 v67, v43, v74
	v_pk_mov_b32 v[42:43], v[92:93], v[90:91] op_sel:[1,0]
	v_mov_b32_e32 v93, v91
	v_pk_add_f32 v[42:43], v[42:43], v[92:93]
	v_pk_mul_f32 v[68:69], v[44:45], v[74:75] op_sel_hi:[1,0]
	v_pk_add_f32 v[42:43], v[42:43], v[42:43] op_sel:[0,1] op_sel_hi:[1,0]
	v_pk_mov_b32 v[44:45], v[106:107], v[88:89] op_sel:[1,0]
	v_mov_b32_e32 v43, v42
	s_nop 1
	v_permlane32_swap_b32_e32 v42, v43
	v_add_f32_e32 v42, v42, v43
	v_rcp_f32_e32 v42, v42
	v_mov_b32_e32 v107, v89
	v_pk_add_f32 v[44:45], v[44:45], v[106:107]
	v_pk_mul_f32 v[72:73], v[48:49], v[74:75] op_sel_hi:[1,0]
	v_pk_add_f32 v[44:45], v[44:45], v[44:45] op_sel:[0,1] op_sel_hi:[1,0]
	v_pk_mul_f32 v[36:37], v[36:37], v[74:75] op_sel_hi:[1,0]
	v_pk_mul_f32 v[38:39], v[38:39], v[74:75] op_sel_hi:[1,0]
	v_pk_mul_f32 v[40:41], v[40:41], v[74:75] op_sel_hi:[1,0]
	v_pk_mul_f32 v[34:35], v[34:35], v[74:75] op_sel_hi:[1,0]
	v_pk_mul_f32 v[74:75], v[58:59], v[42:43] op_sel_hi:[1,0]
	v_pk_mul_f32 v[78:79], v[60:61], v[42:43] op_sel_hi:[1,0]
	v_pk_mul_f32 v[80:81], v[62:63], v[42:43] op_sel_hi:[1,0]
	v_pk_mul_f32 v[82:83], v[64:65], v[42:43] op_sel_hi:[1,0]
	v_pk_mul_f32 v[92:93], v[52:53], v[42:43] op_sel_hi:[1,0]
	v_mov_b32_e32 v43, v44
	s_nop 1
	v_permlane32_swap_b32_e32 v44, v43
	v_add_f32_e32 v43, v44, v43
	v_rcp_f32_e32 v76, v43
	v_pk_mul_f32 v[96:97], v[54:55], v[42:43] op_sel_hi:[1,0]
	v_pk_mul_f32 v[94:95], v[56:57], v[42:43] op_sel_hi:[1,0]
	v_pk_mul_f32 v[98:99], v[50:51], v[42:43] op_sel_hi:[1,0]
	v_pk_mul_f32 v[100:101], v[4:5], v[76:77] op_sel_hi:[1,0]
	v_pk_mov_b32 v[4:5], v[86:87], v[84:85] op_sel:[1,0]
	v_mov_b32_e32 v87, v85
	v_pk_add_f32 v[4:5], v[4:5], v[86:87]
	v_pk_mul_f32 v[102:103], v[6:7], v[76:77] op_sel_hi:[1,0]
	v_pk_add_f32 v[104:105], v[4:5], v[4:5] op_sel:[0,1] op_sel_hi:[1,0]
	v_cvt_pk_bf16_f32 v7, v40, v41
	ds_read_b128 v[84:87], v150 offset:52224
	ds_read_b128 v[50:53], v150 offset:35840
	ds_read_b128 v[54:57], v150 offset:36864
	ds_read_b128 v[58:61], v150 offset:37888
	ds_read_b128 v[62:65], v150 offset:38912
	v_cvt_pk_bf16_f32 v6, v38, v39
	v_cvt_pk_bf16_f32 v5, v36, v37
	v_cvt_pk_bf16_f32 v4, v34, v35
	ds_read_b128 v[88:91], v150 offset:53248
	ds_read_b128 v[34:37], v150 offset:39936
	ds_read_b128 v[38:41], v150 offset:40960
	ds_read_b128 v[42:45], v150 offset:41984
	ds_read_b128 v[46:49], v150 offset:43008
	v_cvt_pk_bf16_f32 v95, v94, v95
	v_cvt_pk_bf16_f32 v94, v96, v97
	v_cvt_pk_bf16_f32 v93, v92, v93
	v_cvt_pk_bf16_f32 v92, v98, v99
	s_waitcnt lgkmcnt(5)
	v_mfma_f32_32x32x16_bf16 v[50:65], v[84:87], v[4:7], v[50:65]
	v_mul_f32_e32 v10, v10, v76
	v_mul_f32_e32 v11, v11, v76
	v_mul_f32_e32 v12, v12, v76
	v_mul_f32_e32 v13, v13, v76
	v_mul_f32_e32 v8, v8, v76
	v_mul_f32_e32 v9, v9, v76
	v_mov_b32_e32 v77, v104
	s_nop 1
	v_permlane32_swap_b32_e32 v104, v77
	v_cvt_pk_bf16_f32 v73, v72, v73
	s_waitcnt lgkmcnt(0)
	v_mfma_f32_32x32x16_bf16 v[34:49], v[84:87], v[92:95], v[34:49]
	v_cvt_pk_bf16_f32 v72, v70, v71
	v_cvt_pk_bf16_f32 v70, v66, v67
	v_add_f32_e32 v66, v104, v77
	v_cvt_pk_bf16_f32 v71, v68, v69
	v_rcp_f32_e32 v104, v66
	v_cvt_pk_bf16_f32 v69, v82, v83
	v_cvt_pk_bf16_f32 v68, v80, v81
	v_cvt_pk_bf16_f32 v67, v78, v79
	v_cvt_pk_bf16_f32 v66, v74, v75
	ds_read_b128 v[78:81], v150 offset:54272
	v_mfma_f32_32x32x16_bf16 v[50:65], v[88:91], v[70:73], v[50:65]
	v_mul_f32_e32 v2, v2, v76
	v_mul_f32_e32 v3, v3, v76
	v_mul_f32_e32 v20, v20, v104
	v_mul_f32_e32 v21, v21, v104
	v_cvt_pk_bf16_f32 v85, v8, v9
	v_cvt_pk_bf16_f32 v82, v2, v3
	v_pk_mul_f32 v[2:3], v[22:23], v[104:105] op_sel_hi:[1,0]
	v_pk_mul_f32 v[8:9], v[24:25], v[104:105] op_sel_hi:[1,0]
	v_pk_mul_f32 v[18:19], v[18:19], v[104:105] op_sel_hi:[1,0]
	v_mfma_f32_32x32x16_bf16 v[34:49], v[88:91], v[66:69], v[34:49]
	v_cvt_pk_bf16_f32 v84, v102, v103
	v_cvt_pk_bf16_f32 v83, v100, v101
	ds_read_b128 v[86:89], v150 offset:55296
	v_cvt_pk_bf16_f32 v99, v8, v9
	v_cvt_pk_bf16_f32 v98, v2, v3
	v_cvt_pk_bf16_f32 v97, v20, v21
	v_cvt_pk_bf16_f32 v96, v18, v19
	s_waitcnt lgkmcnt(1)
	v_mfma_f32_32x32x16_bf16 v[50:65], v[78:81], v[82:85], v[50:65]
	v_mul_f32_e32 v2, v14, v76
	v_mul_f32_e32 v3, v15, v76
	v_mul_f32_e32 v8, v16, v76
	v_mul_f32_e32 v9, v17, v76
	v_mul_f32_e32 v14, v26, v104
	v_mul_f32_e32 v15, v27, v104
	v_cvt_pk_bf16_f32 v77, v8, v9
	v_cvt_pk_bf16_f32 v76, v2, v3
	v_cvt_pk_bf16_f32 v74, v10, v11
	v_pk_mul_f32 v[2:3], v[28:29], v[104:105] op_sel_hi:[1,0]
	v_mfma_f32_32x32x16_bf16 v[34:49], v[78:81], v[96:99], v[34:49]
	v_mul_f32_e32 v8, v30, v104
	v_mul_f32_e32 v9, v31, v104
	v_mul_f32_e32 v10, v32, v104
	v_mul_f32_e32 v11, v33, v104
	v_cvt_pk_bf16_f32 v75, v12, v13
	v_cvt_pk_bf16_f32 v81, v10, v11
	v_cvt_pk_bf16_f32 v80, v8, v9
	v_cvt_pk_bf16_f32 v79, v2, v3
	v_cvt_pk_bf16_f32 v78, v14, v15
	s_waitcnt lgkmcnt(0)
	v_mfma_f32_32x32x16_bf16 v[50:65], v[86:89], v[74:77], v[50:65]
	v_mfma_f32_32x32x16_bf16 v[34:49], v[86:89], v[78:81], v[34:49]
	ds_read_b128 v[86:89], v150 offset:56320
	ds_read_b128 v[18:21], v150 offset:44032
	ds_read_b128 v[22:25], v150 offset:45056
	ds_read_b128 v[26:29], v150 offset:46080
	ds_read_b128 v[30:33], v150 offset:47104
	ds_read_b128 v[100:103], v150 offset:57344
	s_waitcnt lgkmcnt(1)
	v_mfma_f32_32x32x16_bf16 v[18:33], v[86:89], v[4:7], v[18:33]
	ds_read_b128 v[2:5], v150 offset:48128
	ds_read_b128 v[6:9], v150 offset:49152
	ds_read_b128 v[10:13], v150 offset:50176
	ds_read_b128 v[14:17], v150 offset:51200
	s_waitcnt lgkmcnt(0)
	v_mfma_f32_32x32x16_bf16 v[2:17], v[86:89], v[92:95], v[2:17]
	v_mfma_f32_32x32x16_bf16 v[18:33], v[100:103], v[70:73], v[18:33]
	v_mfma_f32_32x32x16_bf16 v[2:17], v[100:103], v[66:69], v[2:17]
	ds_read_b128 v[66:69], v150 offset:58368
	ds_read_b128 v[70:73], v150 offset:59392
	s_waitcnt lgkmcnt(1)
	v_mfma_f32_32x32x16_bf16 v[18:33], v[66:69], v[82:85], v[18:33]
	v_mfma_f32_32x32x16_bf16 v[2:17], v[66:69], v[96:99], v[2:17]
	s_waitcnt lgkmcnt(0)
	v_mfma_f32_32x32x16_bf16 v[18:33], v[70:73], v[74:77], v[18:33]
	v_mfma_f32_32x32x16_bf16 v[2:17], v[70:73], v[78:81], v[2:17]
	s_nop 10
	v_mul_f32_e32 v66, v22, v22
	v_mul_f32_e32 v67, v23, v23
	v_mul_f32_e32 v68, v30, v30
	v_mul_f32_e32 v69, v31, v31
	v_mul_f32_e32 v70, v24, v24
	v_mul_f32_e32 v71, v25, v25
	v_pk_mul_f32 v[72:73], v[32:33], v[32:33]
	v_pk_mul_f32 v[74:75], v[20:21], v[20:21]
	v_pk_mul_f32 v[76:77], v[28:29], v[28:29]
	v_pk_mul_f32 v[78:79], v[26:27], v[26:27]
	v_pk_mul_f32 v[80:81], v[18:19], v[18:19]
	v_pk_fma_f32 v[78:79], v[58:59], v[58:59], v[78:79]
	v_pk_fma_f32 v[76:77], v[60:61], v[60:61], v[76:77]
	v_pk_fma_f32 v[74:75], v[52:53], v[52:53], v[74:75]
	v_pk_fma_f32 v[72:73], v[64:65], v[64:65], v[72:73]
	v_pk_fma_f32 v[70:71], v[56:57], v[56:57], v[70:71]
	v_pk_fma_f32 v[68:69], v[62:63], v[62:63], v[68:69]
	v_pk_fma_f32 v[66:67], v[54:55], v[54:55], v[66:67]
	v_pk_fma_f32 v[80:81], v[50:51], v[50:51], v[80:81]
	v_pk_add_f32 v[66:67], v[66:67], v[68:69]
	v_pk_add_f32 v[68:69], v[70:71], v[72:73]
	v_pk_add_f32 v[70:71], v[74:75], v[76:77]
	v_pk_add_f32 v[72:73], v[80:81], v[78:79]
	v_pk_add_f32 v[68:69], v[70:71], v[68:69]
	v_pk_add_f32 v[66:67], v[72:73], v[66:67]
	v_pk_mul_f32 v[72:73], v[14:15], v[14:15]
	v_pk_mov_b32 v[70:71], v[66:67], v[68:69] op_sel:[1,0]
	v_mov_b32_e32 v67, v69
	v_pk_add_f32 v[66:67], v[70:71], v[66:67]
	v_pk_mul_f32 v[70:71], v[6:7], v[6:7]
	v_pk_mul_f32 v[74:75], v[8:9], v[8:9]
	v_pk_mul_f32 v[76:77], v[16:17], v[16:17]
	v_pk_mul_f32 v[78:79], v[4:5], v[4:5]
	v_pk_mul_f32 v[80:81], v[12:13], v[12:13]
	v_pk_mul_f32 v[82:83], v[10:11], v[10:11]
	v_pk_mul_f32 v[84:85], v[2:3], v[2:3]
	v_pk_fma_f32 v[82:83], v[42:43], v[42:43], v[82:83]
	v_pk_fma_f32 v[80:81], v[44:45], v[44:45], v[80:81]
	v_pk_fma_f32 v[78:79], v[36:37], v[36:37], v[78:79]
	v_pk_fma_f32 v[76:77], v[48:49], v[48:49], v[76:77]
	v_pk_fma_f32 v[74:75], v[40:41], v[40:41], v[74:75]
	v_pk_fma_f32 v[72:73], v[46:47], v[46:47], v[72:73]
	v_pk_fma_f32 v[70:71], v[38:39], v[38:39], v[70:71]
	v_pk_fma_f32 v[84:85], v[34:35], v[34:35], v[84:85]
	v_pk_add_f32 v[70:71], v[70:71], v[72:73]
	v_pk_add_f32 v[72:73], v[74:75], v[76:77]
	v_pk_add_f32 v[74:75], v[78:79], v[80:81]
	v_pk_add_f32 v[76:77], v[84:85], v[82:83]
	v_pk_add_f32 v[72:73], v[74:75], v[72:73]
	v_pk_add_f32 v[70:71], v[76:77], v[70:71]
	v_pk_add_f32 v[66:67], v[66:67], v[66:67] op_sel:[0,1] op_sel_hi:[1,0]
	v_pk_mov_b32 v[74:75], v[70:71], v[72:73] op_sel:[1,0]
	v_mov_b32_e32 v71, v73
	v_pk_add_f32 v[70:71], v[74:75], v[70:71]
	v_mov_b32_e32 v69, v66
	v_pk_add_f32 v[70:71], v[70:71], v[70:71] op_sel:[0,1] op_sel_hi:[1,0]
	s_nop 0
	v_permlane32_swap_b32_e32 v66, v69
	v_mov_b32_e32 v68, v70
	s_nop 1
	v_permlane32_swap_b32_e32 v70, v68
	v_mov_b32_e32 v71, v66
	v_pk_add_f32 v[66:67], v[70:71], v[68:69]
	v_pk_fma_f32 v[66:67], v[66:67], s[0:1], v[152:153] op_sel_hi:[1,0,0]
	s_mov_b32 s1, 0x800000
	v_mul_f32_e32 v68, 0x4b800000, v67
	v_cmp_gt_f32_e32 vcc, s1, v67
	s_nop 1
	v_cndmask_b32_e32 v67, v67, v68, vcc
	v_rsq_f32_e32 v67, v67
	s_nop 0
	v_mul_f32_e32 v68, 0x45800000, v67
	v_cndmask_b32_e32 v68, v67, v68, vcc
	v_pk_mul_f32 v[158:159], v[50:51], v[68:69] op_sel_hi:[1,0]
	v_pk_mul_f32 v[50:51], v[18:19], v[68:69] op_sel_hi:[1,0]
	v_mul_f32_e32 v18, 0x4b800000, v66
	v_cmp_gt_f32_e32 vcc, s1, v66
	v_pk_mul_f32 v[80:81], v[60:61], v[68:69] op_sel_hi:[1,0]
	v_pk_mul_f32 v[60:61], v[28:29], v[68:69] op_sel_hi:[1,0]
	v_cndmask_b32_e32 v18, v66, v18, vcc
	v_rsq_f32_e32 v18, v18
	v_pk_mul_f32 v[78:79], v[58:59], v[68:69] op_sel_hi:[1,0]
	v_pk_mul_f32 v[160:161], v[52:53], v[68:69] op_sel_hi:[1,0]
	v_pk_mul_f32 v[82:83], v[54:55], v[68:69] op_sel_hi:[1,0]
	v_mul_f32_e32 v19, 0x45800000, v18
	v_cndmask_b32_e32 v28, v18, v19, vcc
	v_pk_mul_f32 v[168:169], v[56:57], v[68:69] op_sel_hi:[1,0]
	v_pk_mul_f32 v[58:59], v[26:27], v[68:69] op_sel_hi:[1,0]
	v_pk_mul_f32 v[52:53], v[20:21], v[68:69] op_sel_hi:[1,0]
	v_pk_mul_f32 v[54:55], v[22:23], v[68:69] op_sel_hi:[1,0]
	v_pk_mul_f32 v[56:57], v[24:25], v[68:69] op_sel_hi:[1,0]
	v_pk_mul_f32 v[18:19], v[42:43], v[28:29] op_sel_hi:[1,0]
	v_pk_mul_f32 v[20:21], v[44:45], v[28:29] op_sel_hi:[1,0]
	v_pk_mul_f32 v[22:23], v[46:47], v[28:29] op_sel_hi:[1,0]
	v_pk_mul_f32 v[26:27], v[48:49], v[28:29] op_sel_hi:[1,0]
	v_pk_mul_f32 v[162:163], v[34:35], v[28:29] op_sel_hi:[1,0]
	v_pk_mul_f32 v[164:165], v[36:37], v[28:29] op_sel_hi:[1,0]
	v_pk_mul_f32 v[166:167], v[38:39], v[28:29] op_sel_hi:[1,0]
	v_pk_mul_f32 v[24:25], v[40:41], v[28:29] op_sel_hi:[1,0]
	v_pk_mul_f32 v[104:105], v[2:3], v[28:29] op_sel_hi:[1,0]
	v_pk_mul_f32 v[112:113], v[4:5], v[28:29] op_sel_hi:[1,0]
	ds_read_b128 v[2:5], v150 offset:60416
	ds_read_b128 v[34:37], v174 offset:32768
	ds_read_b128 v[38:41], v174 offset:32800
	ds_read_b128 v[42:45], v174 offset:32832
	ds_read_b128 v[46:49], v174 offset:32864
	v_cvt_pk_bf16_f32 v129, v168, v169
	v_cvt_pk_bf16_f32 v128, v82, v83
	v_cvt_pk_bf16_f32 v127, v160, v161
	v_cvt_pk_bf16_f32 v126, v158, v159
	v_cvt_pk_bf16_f32 v137, v24, v25
	v_cvt_pk_bf16_f32 v136, v166, v167
	v_cvt_pk_bf16_f32 v135, v164, v165
	s_waitcnt lgkmcnt(0)
	v_mfma_f32_32x32x16_bf16 v[86:101], v[2:5], v[126:129], v[34:49]
	v_cvt_pk_bf16_f32 v134, v162, v163
	v_mul_f32_e32 v84, v62, v68
	v_mul_f32_e32 v85, v63, v68
	v_mul_f32_e32 v170, v64, v68
	v_mul_f32_e32 v171, v65, v68
	v_pk_mul_f32 v[62:63], v[30:31], v[68:69] op_sel_hi:[1,0]
	v_pk_mul_f32 v[64:65], v[32:33], v[68:69] op_sel_hi:[1,0]
	v_pk_mul_f32 v[116:117], v[6:7], v[28:29] op_sel_hi:[1,0]
	v_pk_mul_f32 v[154:155], v[8:9], v[28:29] op_sel_hi:[1,0]
	v_mfma_f32_32x32x16_bf16 v[34:49], v[2:5], v[134:137], v[34:49]
	ds_read_b128 v[6:9], v150 offset:61440
	ds_read_b128 v[66:69], v174 offset:32896
	ds_read_b128 v[106:109], v150 offset:64512
	v_cvt_pk_bf16_f32 v125, v170, v171
	v_cvt_pk_bf16_f32 v124, v84, v85
	v_cvt_pk_bf16_f32 v123, v80, v81
	v_cvt_pk_bf16_f32 v122, v78, v79
	v_cvt_pk_bf16_f32 v149, v26, v27
	v_cvt_pk_bf16_f32 v148, v22, v23
	v_cvt_pk_bf16_f32 v147, v20, v21
	v_cvt_pk_bf16_f32 v146, v18, v19
	s_waitcnt lgkmcnt(2)
	v_mfma_f32_32x32x16_bf16 v[86:101], v[6:9], v[122:125], v[86:101]
	v_mul_f32_e32 v102, v10, v28
	v_mul_f32_e32 v103, v11, v28
	v_mul_f32_e32 v110, v12, v28
	v_mul_f32_e32 v111, v13, v28
	v_mul_f32_e32 v114, v14, v28
	v_mul_f32_e32 v115, v15, v28
	v_pk_mul_f32 v[156:157], v[16:17], v[28:29] op_sel_hi:[1,0]
	ds_read_b128 v[176:179], v174 offset:33536
	ds_read_b128 v[180:183], v174 offset:33568
	ds_read_b128 v[184:187], v174 offset:33600
	ds_read_b128 v[28:31], v174 offset:33632
	ds_read_b128 v[188:191], v174 offset:33792
	ds_read_b128 v[192:195], v174 offset:33824
	ds_read_b128 v[196:199], v174 offset:33856
	ds_read_b128 v[200:203], v174 offset:33888
	ds_read_b128 v[204:207], v150 offset:62464
	v_cvt_pk_bf16_f32 v133, v56, v57
	v_mfma_f32_32x32x16_bf16 v[34:49], v[6:9], v[146:149], v[34:49]
	v_cvt_pk_bf16_f32 v132, v54, v55
	v_cvt_pk_bf16_f32 v131, v52, v53
	v_cvt_pk_bf16_f32 v130, v50, v51
	ds_read_b128 v[70:73], v174 offset:33664
	ds_read_b128 v[74:77], v174 offset:33920
	ds_read_b128 v[208:211], v150 offset:63488
	v_cvt_pk_bf16_f32 v145, v154, v155
	v_cvt_pk_bf16_f32 v144, v116, v117
	v_cvt_pk_bf16_f32 v143, v112, v113
	v_cvt_pk_bf16_f32 v142, v104, v105
	s_waitcnt lgkmcnt(3)
	v_mfma_f32_32x32x16_bf16 v[86:101], v[204:207], v[130:133], v[86:101]
	v_cvt_pk_bf16_f32 v121, v64, v65
	v_cvt_pk_bf16_f32 v120, v62, v63
	v_cvt_pk_bf16_f32 v119, v60, v61
	v_cvt_pk_bf16_f32 v118, v58, v59
	v_cvt_pk_bf16_f32 v141, v156, v157
	v_cvt_pk_bf16_f32 v140, v114, v115
	v_cvt_pk_bf16_f32 v139, v110, v111
	v_mfma_f32_32x32x16_bf16 v[34:49], v[204:207], v[142:145], v[34:49]
	v_cvt_pk_bf16_f32 v138, v102, v103
	v_fma_f32 v16, v30, v170, v202
	v_fma_f32 v17, v31, v171, v203
	v_fma_f32 v14, v28, v84, v200
	v_fma_f32 v15, v29, v85, v201
	v_pk_fma_f32 v[12:13], v[186:187], v[80:81], v[198:199]
	v_pk_fma_f32 v[10:11], v[184:185], v[78:79], v[196:197]
	v_pk_fma_f32 v[8:9], v[182:183], v[168:169], v[194:195]
	s_waitcnt lgkmcnt(0)
	v_mfma_f32_32x32x16_bf16 v[86:101], v[208:211], v[118:121], v[86:101]
	v_fma_f32 v6, v180, v82, v192
	v_fma_f32 v7, v181, v83, v193
	ds_read_b128 v[78:81], v174 offset:33760
	ds_read_b128 v[82:85], v174 offset:33248
	v_fma_f32 v4, v178, v160, v190
	v_fma_f32 v5, v179, v161, v191
	v_pk_fma_f32 v[2:3], v[176:177], v[158:159], v[188:189]
	v_pk_fma_f32 v[32:33], v[30:31], v[26:27], v[202:203]
	v_pk_fma_f32 v[30:31], v[28:29], v[22:23], v[200:201]
	v_pk_fma_f32 v[28:29], v[186:187], v[20:21], v[198:199]
	v_pk_fma_f32 v[26:27], v[184:185], v[18:19], v[196:197]
	v_pk_fma_f32 v[24:25], v[182:183], v[24:25], v[194:195]
	v_pk_fma_f32 v[22:23], v[180:181], v[166:167], v[192:193]
	v_pk_fma_f32 v[20:21], v[178:179], v[164:165], v[190:191]
	v_pk_fma_f32 v[18:19], v[176:177], v[162:163], v[188:189]
	ds_read_b128 v[158:161], v174 offset:33696
	ds_read_b128 v[162:165], v174 offset:33728
	ds_read_b128 v[166:169], v174 offset:33952
	ds_read_b128 v[176:179], v174 offset:33984
	ds_read_b128 v[180:183], v174 offset:34016
	ds_read_b128 v[184:187], v212 offset:11264
	v_mfma_f32_32x32x16_bf16 v[34:49], v[208:211], v[138:141], v[34:49]
	v_cvt_pk_bf16_f32 v86, v86, v87
	v_cvt_pk_bf16_f32 v87, v88, v89
	v_cvt_pk_bf16_f32 v88, v90, v91
	v_cvt_pk_bf16_f32 v89, v92, v93
	ds_read_b128 v[90:93], v212 offset:12288
	v_pk_max_i16 v86, v86, 0
	v_pk_max_i16 v87, v87, 0
	v_pk_max_i16 v88, v88, 0
	v_pk_max_i16 v89, v89, 0
	s_nop 1
	s_nop 0
	v_cvt_pk_bf16_f32 v188, v34, v35
	v_cvt_pk_bf16_f32 v189, v36, v37
	v_cvt_pk_bf16_f32 v190, v38, v39
	v_cvt_pk_bf16_f32 v191, v40, v41
	s_waitcnt lgkmcnt(1)
	v_mfma_f32_32x32x16_bf16 v[2:17], v[184:187], v[86:89], v[2:17]
	v_pk_max_i16 v188, v188, 0
	v_pk_max_i16 v189, v189, 0
	v_pk_max_i16 v190, v190, 0
	v_pk_max_i16 v191, v191, 0
	v_cvt_pk_bf16_f32 v94, v94, v95
	v_cvt_pk_bf16_f32 v95, v96, v97
	v_cvt_pk_bf16_f32 v96, v98, v99
	v_cvt_pk_bf16_f32 v97, v100, v101
	v_cvt_pk_bf16_f32 v98, v42, v43
	v_cvt_pk_bf16_f32 v99, v44, v45
	v_mfma_f32_32x32x16_bf16 v[18:33], v[184:187], v[188:191], v[18:33]
	ds_read_b128 v[184:187], v212 offset:19456
	v_cvt_pk_bf16_f32 v100, v46, v47
	v_cvt_pk_bf16_f32 v101, v48, v49
	v_fma_f32 v64, v80, v64, v182
	v_fma_f32 v65, v81, v65, v183
	v_pk_fma_f32 v[62:63], v[78:79], v[62:63], v[180:181]
	v_pk_fma_f32 v[60:61], v[164:165], v[60:61], v[178:179]
	v_pk_fma_f32 v[58:59], v[162:163], v[58:59], v[176:177]
	v_pk_max_i16 v94, v94, 0
	v_pk_max_i16 v95, v95, 0
	v_pk_max_i16 v96, v96, 0
	v_pk_max_i16 v97, v97, 0
	v_pk_max_i16 v98, v98, 0
	v_pk_max_i16 v99, v99, 0
	v_pk_max_i16 v100, v100, 0
	v_pk_max_i16 v101, v101, 0
	v_pk_fma_f32 v[56:57], v[160:161], v[56:57], v[168:169]
	s_waitcnt lgkmcnt(1)
	v_mfma_f32_32x32x16_bf16 v[2:17], v[90:93], v[94:97], v[2:17]
	v_fma_f32 v54, v158, v54, v166
	v_fma_f32 v55, v159, v55, v167
	v_fma_f32 v52, v72, v52, v76
	v_fma_f32 v53, v73, v53, v77
	v_fma_f32 v50, v70, v50, v74
	v_fma_f32 v51, v71, v51, v75
	v_pk_fma_f32 v[48:49], v[80:81], v[156:157], v[182:183]
	v_pk_fma_f32 v[46:47], v[78:79], v[114:115], v[180:181]
	v_pk_fma_f32 v[44:45], v[164:165], v[110:111], v[178:179]
	v_pk_fma_f32 v[42:43], v[162:163], v[102:103], v[176:177]
	v_mfma_f32_32x32x16_bf16 v[18:33], v[90:93], v[98:101], v[18:33]
	ds_read_b128 v[90:93], v212 offset:20480
	v_fma_f32 v40, v160, v154, v168
	v_fma_f32 v41, v161, v155, v169
	v_fma_f32 v38, v158, v116, v166
	v_fma_f32 v39, v159, v117, v167
	v_pk_fma_f32 v[36:37], v[72:73], v[112:113], v[76:77]
	v_pk_fma_f32 v[34:35], v[70:71], v[104:105], v[74:75]
	s_waitcnt lgkmcnt(1)
	v_mfma_f32_32x32x16_bf16 v[50:65], v[184:187], v[86:89], v[50:65]
	ds_read_b128 v[70:73], v174 offset:32928
	ds_read_b128 v[74:77], v174 offset:32960
	ds_read_b128 v[78:81], v174 offset:32992
	ds_read_b128 v[86:89], v174 offset:33024
	ds_read_b128 v[110:113], v212 offset:1024
	v_mfma_f32_32x32x16_bf16 v[34:49], v[184:187], v[188:191], v[34:49]
	s_waitcnt lgkmcnt(5)
	v_mfma_f32_32x32x16_bf16 v[50:65], v[90:93], v[94:97], v[50:65]
	v_mfma_f32_32x32x16_bf16 v[34:49], v[90:93], v[98:101], v[34:49]
	s_waitcnt lgkmcnt(2)
	v_mfma_f32_32x32x16_bf16 v[90:105], v[106:109], v[126:129], v[66:81]
	v_mfma_f32_32x32x16_bf16 v[66:81], v[106:109], v[134:137], v[66:81]
	ds_read_b128 v[106:109], v212 offset:0
	s_waitcnt lgkmcnt(0)
	v_mfma_f32_32x32x16_bf16 v[90:105], v[106:109], v[122:125], v[90:105]
	v_mfma_f32_32x32x16_bf16 v[66:81], v[106:109], v[146:149], v[66:81]
	ds_read_b128 v[106:109], v212 offset:2048
	v_mfma_f32_32x32x16_bf16 v[90:105], v[110:113], v[130:133], v[90:105]
	v_mfma_f32_32x32x16_bf16 v[66:81], v[110:113], v[142:145], v[66:81]
	ds_read_b128 v[110:113], v212 offset:13312
	s_waitcnt lgkmcnt(1)
	v_mfma_f32_32x32x16_bf16 v[90:105], v[106:109], v[118:121], v[90:105]
	v_mfma_f32_32x32x16_bf16 v[66:81], v[106:109], v[138:141], v[66:81]
	s_nop 10
	v_cvt_pk_bf16_f32 v90, v90, v91
	v_cvt_pk_bf16_f32 v91, v92, v93
	v_cvt_pk_bf16_f32 v92, v94, v95
	v_cvt_pk_bf16_f32 v94, v98, v99
	v_cvt_pk_bf16_f32 v95, v100, v101
	ds_read_b128 v[98:101], v212 offset:21504
	v_cvt_pk_bf16_f32 v66, v66, v67
	v_cvt_pk_bf16_f32 v67, v68, v69
	v_cvt_pk_bf16_f32 v68, v70, v71
	v_cvt_pk_bf16_f32 v93, v96, v97
	v_cvt_pk_bf16_f32 v69, v72, v73
	ds_read_b128 v[70:73], v212 offset:14336
	v_pk_max_i16 v90, v90, 0
	v_pk_max_i16 v91, v91, 0
	v_pk_max_i16 v92, v92, 0
	v_pk_max_i16 v93, v93, 0
	v_pk_max_i16 v66, v66, 0
	v_pk_max_i16 v67, v67, 0
	v_pk_max_i16 v68, v68, 0
	v_pk_max_i16 v69, v69, 0
	v_cvt_pk_bf16_f32 v96, v102, v103
	s_waitcnt lgkmcnt(2)
	v_mfma_f32_32x32x16_bf16 v[2:17], v[110:113], v[90:93], v[2:17]
	v_cvt_pk_bf16_f32 v97, v104, v105
	v_cvt_pk_bf16_f32 v74, v74, v75
	v_cvt_pk_bf16_f32 v75, v76, v77
	v_cvt_pk_bf16_f32 v76, v78, v79
	v_cvt_pk_bf16_f32 v77, v80, v81
	v_pk_max_i16 v94, v94, 0
	v_pk_max_i16 v95, v95, 0
	v_pk_max_i16 v96, v96, 0
	v_pk_max_i16 v97, v97, 0
	v_pk_max_i16 v74, v74, 0
	v_pk_max_i16 v75, v75, 0
	v_pk_max_i16 v76, v76, 0
	v_pk_max_i16 v77, v77, 0
	v_mfma_f32_32x32x16_bf16 v[18:33], v[110:113], v[66:69], v[18:33]
	s_waitcnt lgkmcnt(1)
	v_mfma_f32_32x32x16_bf16 v[34:49], v[98:101], v[66:69], v[34:49]
	ds_read_b128 v[66:69], v212 offset:22528
	v_mfma_f32_32x32x16_bf16 v[50:65], v[98:101], v[90:93], v[50:65]
	s_waitcnt lgkmcnt(1)
	v_mfma_f32_32x32x16_bf16 v[2:17], v[70:73], v[94:97], v[2:17]
	v_mfma_f32_32x32x16_bf16 v[18:33], v[70:73], v[74:77], v[18:33]
	ds_read_b128 v[78:81], v212 offset:3072
	s_waitcnt lgkmcnt(1)
	v_mfma_f32_32x32x16_bf16 v[50:65], v[66:69], v[94:97], v[50:65]
	ds_read_b128 v[90:93], v174 offset:33056
	ds_read_b128 v[94:97], v174 offset:33088
	ds_read_b128 v[98:101], v174 offset:33120
	ds_read_b128 v[70:73], v174 offset:33152
	v_mfma_f32_32x32x16_bf16 v[34:49], v[66:69], v[74:77], v[34:49]
	ds_read_b128 v[66:69], v212 offset:4096
	ds_read_b128 v[74:77], v212 offset:5120
	s_waitcnt lgkmcnt(3)
	v_mfma_f32_32x32x16_bf16 v[102:117], v[78:81], v[126:129], v[86:101]
	v_mfma_f32_32x32x16_bf16 v[86:101], v[78:81], v[134:137], v[86:101]
	s_waitcnt lgkmcnt(1)
	v_mfma_f32_32x32x16_bf16 v[86:101], v[66:69], v[146:149], v[86:101]
	v_mfma_f32_32x32x16_bf16 v[102:117], v[66:69], v[122:125], v[102:117]
	ds_read_b128 v[66:69], v212 offset:6144
	s_waitcnt lgkmcnt(1)
	v_mfma_f32_32x32x16_bf16 v[86:101], v[74:77], v[142:145], v[86:101]
	v_mfma_f32_32x32x16_bf16 v[102:117], v[74:77], v[130:133], v[102:117]
	ds_read_b128 v[74:77], v212 offset:15360
	s_waitcnt lgkmcnt(1)
	v_mfma_f32_32x32x16_bf16 v[86:101], v[66:69], v[138:141], v[86:101]
	v_mfma_f32_32x32x16_bf16 v[102:117], v[66:69], v[118:121], v[102:117]
	s_nop 10
	v_cvt_pk_bf16_f32 v78, v86, v87
	v_cvt_pk_bf16_f32 v80, v90, v91
	v_cvt_pk_bf16_f32 v79, v88, v89
	v_cvt_pk_bf16_f32 v81, v92, v93
	ds_read_b128 v[86:89], v212 offset:16384
	ds_read_b128 v[90:93], v212 offset:23552
	v_cvt_pk_bf16_f32 v66, v102, v103
	v_cvt_pk_bf16_f32 v67, v104, v105
	v_cvt_pk_bf16_f32 v68, v106, v107
	v_cvt_pk_bf16_f32 v69, v108, v109
	v_pk_max_i16 v66, v66, 0
	v_pk_max_i16 v67, v67, 0
	v_pk_max_i16 v68, v68, 0
	v_pk_max_i16 v69, v69, 0
	v_pk_max_i16 v78, v78, 0
	v_pk_max_i16 v79, v79, 0
	v_pk_max_i16 v80, v80, 0
	v_pk_max_i16 v81, v81, 0
	v_cvt_pk_bf16_f32 v94, v94, v95
	s_waitcnt lgkmcnt(2)
	v_mfma_f32_32x32x16_bf16 v[18:33], v[74:77], v[78:81], v[18:33]
	v_cvt_pk_bf16_f32 v95, v96, v97
	v_cvt_pk_bf16_f32 v96, v98, v99
	v_cvt_pk_bf16_f32 v97, v100, v101
	v_pk_max_i16 v94, v94, 0
	v_pk_max_i16 v95, v95, 0
	v_pk_max_i16 v96, v96, 0
	v_pk_max_i16 v97, v97, 0
	v_mfma_f32_32x32x16_bf16 v[2:17], v[74:77], v[66:69], v[2:17]
	v_cvt_pk_bf16_f32 v74, v110, v111
	v_cvt_pk_bf16_f32 v75, v112, v113
	v_cvt_pk_bf16_f32 v76, v114, v115
	v_cvt_pk_bf16_f32 v77, v116, v117
	v_pk_max_i16 v74, v74, 0
	v_pk_max_i16 v75, v75, 0
	v_pk_max_i16 v76, v76, 0
	v_pk_max_i16 v77, v77, 0
	s_waitcnt lgkmcnt(0)
	v_mfma_f32_32x32x16_bf16 v[50:65], v[90:93], v[66:69], v[50:65]
	ds_read_b128 v[66:69], v212 offset:24576
	v_mfma_f32_32x32x16_bf16 v[34:49], v[90:93], v[78:81], v[34:49]
	ds_read_b128 v[102:105], v212 offset:7168
	v_mfma_f32_32x32x16_bf16 v[2:17], v[86:89], v[74:77], v[2:17]
	s_waitcnt lgkmcnt(1)
	v_mfma_f32_32x32x16_bf16 v[50:65], v[66:69], v[74:77], v[50:65]
	ds_read_b128 v[74:77], v174 offset:33184
	ds_read_b128 v[78:81], v174 offset:33216
	v_mfma_f32_32x32x16_bf16 v[34:49], v[66:69], v[94:97], v[34:49]
	ds_read_b128 v[66:69], v212 offset:8192
	v_mfma_f32_32x32x16_bf16 v[18:33], v[86:89], v[94:97], v[18:33]
	s_waitcnt lgkmcnt(1)
	v_mfma_f32_32x32x16_bf16 v[86:101], v[102:105], v[126:129], v[70:85]
	v_mfma_f32_32x32x16_bf16 v[70:85], v[102:105], v[134:137], v[70:85]
	ds_read_b128 v[102:105], v212 offset:9216
	v_lshlrev_b32_e32 v135, 2, v1
	v_add_u32_e32 v134, v172, v174
	s_waitcnt lgkmcnt(1)
	v_mfma_f32_32x32x16_bf16 v[86:101], v[66:69], v[122:125], v[86:101]
	v_mfma_f32_32x32x16_bf16 v[70:85], v[66:69], v[146:149], v[70:85]
	ds_read_b128 v[66:69], v212 offset:10240
	s_waitcnt lgkmcnt(1)
	v_mfma_f32_32x32x16_bf16 v[86:101], v[102:105], v[130:133], v[86:101]
	v_mfma_f32_32x32x16_bf16 v[70:85], v[102:105], v[142:145], v[70:85]
	ds_read_b128 v[102:105], v212 offset:17408
	s_waitcnt lgkmcnt(1)
	v_mfma_f32_32x32x16_bf16 v[86:101], v[66:69], v[118:121], v[86:101]
	v_mfma_f32_32x32x16_bf16 v[70:85], v[66:69], v[138:141], v[70:85]
	s_nop 10
	v_cvt_pk_bf16_f32 v68, v90, v91
	v_cvt_pk_bf16_f32 v69, v92, v93
	ds_read_b128 v[90:93], v212 offset:25600
	v_cvt_pk_bf16_f32 v66, v86, v87
	v_cvt_pk_bf16_f32 v67, v88, v89
	v_pk_max_i16 v66, v66, 0
	v_pk_max_i16 v67, v67, 0
	v_pk_max_i16 v68, v68, 0
	v_pk_max_i16 v69, v69, 0
	v_cvt_pk_bf16_f32 v70, v70, v71
	v_cvt_pk_bf16_f32 v71, v72, v73
	s_waitcnt lgkmcnt(1)
	v_mfma_f32_32x32x16_bf16 v[2:17], v[102:105], v[66:69], v[2:17]
	v_cvt_pk_bf16_f32 v72, v74, v75
	v_cvt_pk_bf16_f32 v73, v76, v77
	ds_read_b128 v[74:77], v212 offset:18432
	v_cvt_pk_bf16_f32 v86, v94, v95
	v_cvt_pk_bf16_f32 v87, v96, v97
	v_cvt_pk_bf16_f32 v88, v98, v99
	s_waitcnt lgkmcnt(1)
	v_mfma_f32_32x32x16_bf16 v[50:65], v[90:93], v[66:69], v[50:65]
	ds_read_b128 v[66:69], v212 offset:26624
	v_cvt_pk_bf16_f32 v89, v100, v101
	v_pk_max_i16 v86, v86, 0
	v_pk_max_i16 v87, v87, 0
	v_pk_max_i16 v88, v88, 0
	v_pk_max_i16 v89, v89, 0
	v_pk_max_i16 v70, v70, 0
	v_pk_max_i16 v71, v71, 0
	v_pk_max_i16 v72, v72, 0
	v_pk_max_i16 v73, v73, 0
	v_cvt_pk_bf16_f32 v78, v78, v79
	v_cvt_pk_bf16_f32 v79, v80, v81
	s_waitcnt lgkmcnt(1)
	v_mfma_f32_32x32x16_bf16 v[2:17], v[74:77], v[86:89], v[2:17]
	v_cvt_pk_bf16_f32 v80, v82, v83
	v_cvt_pk_bf16_f32 v81, v84, v85
	v_pk_max_i16 v78, v78, 0
	v_pk_max_i16 v79, v79, 0
	v_pk_max_i16 v80, v80, 0
	v_pk_max_i16 v81, v81, 0
	s_waitcnt lgkmcnt(0)
	v_mfma_f32_32x32x16_bf16 v[50:65], v[66:69], v[86:89], v[50:65]
	v_mfma_f32_32x32x16_bf16 v[34:49], v[90:93], v[70:73], v[34:49]
	s_nop 10
	v_add_f32_e32 v130, v10, v58
	v_add_f32_e32 v131, v11, v59
	v_add_f32_e32 v132, v12, v60
	v_add_f32_e32 v133, v13, v61
	v_add_f32_e32 v138, v4, v52
	v_add_f32_e32 v139, v5, v53
	v_pk_add_f32 v[140:141], v[16:17], v[64:65]
	v_pk_add_f32 v[142:143], v[8:9], v[56:57]
	v_pk_add_f32 v[144:145], v[14:15], v[62:63]
	v_pk_add_f32 v[146:147], v[6:7], v[54:55]
	v_mfma_f32_32x32x16_bf16 v[18:33], v[102:105], v[70:73], v[18:33]
	ds_read2st64_b32 v[70:71], v135 offset0:133 offset1:134
	v_add_f32_e32 v148, v2, v50
	v_add_f32_e32 v149, v3, v51
	v_add_f32_e32 v144, v146, v144
	v_add_f32_e32 v145, v147, v145
	v_pk_add_f32 v[140:141], v[142:143], v[140:141]
	v_pk_add_f32 v[132:133], v[138:139], v[132:133]
	v_pk_add_f32 v[130:131], v[148:149], v[130:131]
	v_pk_add_f32 v[132:133], v[132:133], v[140:141]
	v_pk_add_f32 v[130:131], v[130:131], v[144:145]
	v_mfma_f32_32x32x16_bf16 v[34:49], v[66:69], v[78:81], v[34:49]
	v_pk_mov_b32 v[138:139], v[130:131], v[132:133] op_sel:[1,0]
	v_mov_b32_e32 v131, v133
	s_waitcnt vmcnt(0) lgkmcnt(0)
	v_mul_f32_e32 v66, v175, v70
	v_pk_add_f32 v[130:131], v[138:139], v[130:131]
	ds_write_b32 v173, v66 offset:512
	v_mul_f32_e32 v66, v175, v71
	v_pk_add_f32 v[130:131], v[130:131], v[130:131] op_sel:[0,1] op_sel_hi:[1,0]
	s_waitcnt lgkmcnt(0)
	ds_read_b128 v[102:105], v174 offset:34560
	ds_read_b128 v[98:101], v174 offset:34592
	ds_read_b128 v[110:113], v174 offset:34624
	ds_read_b128 v[106:109], v174 offset:34656
	ds_read_b128 v[114:117], v174 offset:34688
	ds_read_b128 v[122:125], v174 offset:34720
	ds_read_b128 v[118:121], v174 offset:34752
	ds_read_b128 v[126:129], v174 offset:34784
	v_mov_b32_dpp v66, v66 quad_perm:[1,0,3,2] row_mask:0xf bank_mask:0xf bound_ctrl:1
	v_mov_b32_e32 v131, v130
	v_fmac_f32_e32 v66, v175, v71
	s_nop 0
	v_permlane32_swap_b32_e32 v130, v131
	v_add_f32_dpp v66, v66, v66 quad_perm:[2,3,0,1] row_mask:0xf bank_mask:0xf bound_ctrl:1
	v_add_f32_e32 v130, v130, v131
	v_fmamk_f32 v65, v130, 0xbc800000, v65
	v_add_f32_dpp v66, v66, v66 row_half_mirror row_mask:0xf bank_mask:0xf bound_ctrl:1
	v_fmamk_f32 v64, v130, 0xbc800000, v64
	v_fmamk_f32 v63, v130, 0xbc800000, v63
	v_fmamk_f32 v62, v130, 0xbc800000, v62
	v_fmamk_f32 v61, v130, 0xbc800000, v61
	v_fmamk_f32 v60, v130, 0xbc800000, v60
	v_fmamk_f32 v59, v130, 0xbc800000, v59
	v_fmamk_f32 v58, v130, 0xbc800000, v58
	v_fmamk_f32 v57, v130, 0xbc800000, v57
	v_fmamk_f32 v56, v130, 0xbc800000, v56
	v_fmamk_f32 v55, v130, 0xbc800000, v55
	v_fmamk_f32 v54, v130, 0xbc800000, v54
	v_fmamk_f32 v53, v130, 0xbc800000, v53
	v_fmamk_f32 v52, v130, 0xbc800000, v52
	v_fmamk_f32 v51, v130, 0xbc800000, v51
	v_fmac_f32_e32 v50, 0xbc800000, v130
	v_add_f32_dpp v66, v66, v66 row_ror:8 row_mask:0xf bank_mask:0xf bound_ctrl:1
	v_fmamk_f32 v17, v130, 0xbc800000, v17
	v_fmamk_f32 v16, v130, 0xbc800000, v16
	v_fmamk_f32 v15, v130, 0xbc800000, v15
	v_fmamk_f32 v14, v130, 0xbc800000, v14
	v_fmamk_f32 v13, v130, 0xbc800000, v13
	v_fmamk_f32 v12, v130, 0xbc800000, v12
	v_fmamk_f32 v11, v130, 0xbc800000, v11
	v_fmamk_f32 v10, v130, 0xbc800000, v10
	v_fmamk_f32 v9, v130, 0xbc800000, v9
	v_fmamk_f32 v8, v130, 0xbc800000, v8
	v_fmamk_f32 v7, v130, 0xbc800000, v7
	v_fmamk_f32 v6, v130, 0xbc800000, v6
	v_fmamk_f32 v5, v130, 0xbc800000, v5
	v_fmamk_f32 v4, v130, 0xbc800000, v4
	v_fmamk_f32 v3, v130, 0xbc800000, v3
	v_fmac_f32_e32 v2, 0xbc800000, v130
	v_pk_mul_f32 v[130:131], v[54:55], v[54:55]
	v_pk_mul_f32 v[132:133], v[62:63], v[62:63]
	v_pk_mul_f32 v[138:139], v[50:51], v[50:51]
	v_pk_mul_f32 v[140:141], v[58:59], v[58:59]
	v_pk_mul_f32 v[142:143], v[56:57], v[56:57]
	v_pk_mul_f32 v[144:145], v[64:65], v[64:65]
	v_pk_mul_f32 v[146:147], v[52:53], v[52:53]
	v_pk_mul_f32 v[148:149], v[60:61], v[60:61]
	v_mov_b32_e32 v67, v66
	v_pk_fma_f32 v[148:149], v[12:13], v[12:13], v[148:149]
	v_pk_fma_f32 v[146:147], v[4:5], v[4:5], v[146:147]
	v_pk_fma_f32 v[144:145], v[16:17], v[16:17], v[144:145]
	v_pk_fma_f32 v[142:143], v[8:9], v[8:9], v[142:143]
	v_pk_fma_f32 v[140:141], v[10:11], v[10:11], v[140:141]
	v_pk_fma_f32 v[138:139], v[2:3], v[2:3], v[138:139]
	v_pk_fma_f32 v[132:133], v[14:15], v[14:15], v[132:133]
	v_pk_fma_f32 v[130:131], v[6:7], v[6:7], v[130:131]
	v_permlane16_swap_b32_e32 v66, v67
	v_pk_add_f32 v[130:131], v[130:131], v[132:133]
	v_pk_add_f32 v[132:133], v[138:139], v[140:141]
	v_pk_add_f32 v[138:139], v[142:143], v[144:145]
	v_pk_add_f32 v[140:141], v[146:147], v[148:149]
	v_mfma_f32_32x32x16_bf16 v[18:33], v[74:77], v[78:81], v[18:33]
	v_add_f32_e32 v136, v66, v67
	ds_read_b128 v[70:73], v134 offset:512
	ds_read_b128 v[66:69], v134 offset:544
	ds_read_b128 v[78:81], v134 offset:576
	ds_read_b128 v[74:77], v134 offset:608
	ds_read_b128 v[82:85], v134 offset:640
	ds_read_b128 v[90:93], v134 offset:672
	ds_read_b128 v[86:89], v134 offset:704
	ds_read_b128 v[94:97], v134 offset:736
	v_pk_add_f32 v[138:139], v[140:141], v[138:139]
	v_pk_add_f32 v[130:131], v[132:133], v[130:131]
	s_waitcnt lgkmcnt(8)
	v_pk_mul_f32 v[140:141], v[126:127], v[62:63]
	v_pk_mov_b32 v[132:133], v[130:131], v[138:139] op_sel:[1,0]
	v_mov_b32_e32 v131, v139
	v_pk_mul_f32 v[138:139], v[122:123], v[54:55]
	v_pk_mul_f32 v[142:143], v[114:115], v[50:51]
	v_pk_mul_f32 v[144:145], v[118:119], v[58:59]
	v_pk_mul_f32 v[146:147], v[124:125], v[56:57]
	v_pk_mul_f32 v[148:149], v[128:129], v[64:65]
	v_pk_mul_f32 v[154:155], v[116:117], v[52:53]
	v_pk_mul_f32 v[156:157], v[120:121], v[60:61]
	v_pk_fma_f32 v[154:155], v[104:105], v[4:5], v[154:155]
	v_pk_fma_f32 v[156:157], v[112:113], v[12:13], v[156:157]
	v_pk_fma_f32 v[148:149], v[108:109], v[16:17], v[148:149]
	v_pk_fma_f32 v[146:147], v[100:101], v[8:9], v[146:147]
	v_pk_fma_f32 v[144:145], v[110:111], v[10:11], v[144:145]
	v_pk_fma_f32 v[142:143], v[102:103], v[2:3], v[142:143]
	v_pk_fma_f32 v[140:141], v[106:107], v[14:15], v[140:141]
	v_pk_fma_f32 v[138:139], v[98:99], v[6:7], v[138:139]
	v_pk_add_f32 v[130:131], v[132:133], v[130:131]
	v_pk_add_f32 v[138:139], v[138:139], v[140:141]
	v_pk_add_f32 v[140:141], v[142:143], v[144:145]
	v_pk_add_f32 v[142:143], v[146:147], v[148:149]
	v_pk_add_f32 v[144:145], v[154:155], v[156:157]
	v_pk_add_f32 v[132:133], v[130:131], v[130:131] op_sel:[0,1] op_sel_hi:[1,0]
	v_pk_add_f32 v[142:143], v[144:145], v[142:143]
	v_pk_add_f32 v[138:139], v[140:141], v[138:139]
	v_add_f32_e32 v133, v142, v143
	v_add_f32_e32 v130, v138, v139
	s_waitcnt lgkmcnt(2)
	v_pk_mul_f32 v[138:139], v[90:91], v[54:55]
	s_waitcnt lgkmcnt(0)
	v_pk_mul_f32 v[140:141], v[94:95], v[62:63]
	v_pk_mul_f32 v[142:143], v[82:83], v[50:51]
	v_pk_mul_f32 v[144:145], v[86:87], v[58:59]
	v_pk_mul_f32 v[146:147], v[92:93], v[56:57]
	v_pk_mul_f32 v[148:149], v[96:97], v[64:65]
	v_pk_mul_f32 v[154:155], v[84:85], v[52:53]
	v_pk_mul_f32 v[156:157], v[88:89], v[60:61]
	v_add_f32_e32 v130, v130, v133
	v_pk_fma_f32 v[156:157], v[80:81], v[12:13], v[156:157]
	v_pk_fma_f32 v[154:155], v[72:73], v[4:5], v[154:155]
	v_pk_fma_f32 v[148:149], v[76:77], v[16:17], v[148:149]
	v_pk_fma_f32 v[146:147], v[68:69], v[8:9], v[146:147]
	v_pk_fma_f32 v[144:145], v[78:79], v[10:11], v[144:145]
	v_pk_fma_f32 v[142:143], v[70:71], v[2:3], v[142:143]
	v_pk_fma_f32 v[140:141], v[74:75], v[14:15], v[140:141]
	v_pk_fma_f32 v[138:139], v[66:67], v[6:7], v[138:139]
	v_mov_b32_e32 v133, v130
	v_pk_add_f32 v[138:139], v[138:139], v[140:141]
	v_pk_add_f32 v[140:141], v[142:143], v[144:145]
	v_pk_add_f32 v[142:143], v[146:147], v[148:149]
	v_pk_add_f32 v[144:145], v[154:155], v[156:157]
	v_permlane32_swap_b32_e32 v130, v133
	v_pk_add_f32 v[142:143], v[144:145], v[142:143]
	v_add_f32_e32 v160, v130, v133
	v_pk_add_f32 v[138:139], v[140:141], v[138:139]
	v_add_f32_e32 v133, v142, v143
	v_pk_add_f32 v[140:141], v[26:27], v[42:43]
	v_pk_add_f32 v[142:143], v[28:29], v[44:45]
	v_pk_add_f32 v[144:145], v[20:21], v[36:37]
	v_pk_add_f32 v[146:147], v[32:33], v[48:49]
	v_pk_add_f32 v[148:149], v[24:25], v[40:41]
	v_pk_add_f32 v[154:155], v[30:31], v[46:47]
	v_pk_add_f32 v[156:157], v[22:23], v[38:39]
	v_pk_add_f32 v[158:159], v[18:19], v[34:35]
	v_pk_add_f32 v[154:155], v[156:157], v[154:155]
	v_pk_add_f32 v[146:147], v[148:149], v[146:147]
	v_pk_add_f32 v[142:143], v[144:145], v[142:143]
	v_pk_add_f32 v[140:141], v[158:159], v[140:141]
	v_pk_add_f32 v[142:143], v[142:143], v[146:147]
	v_pk_add_f32 v[140:141], v[140:141], v[154:155]
	v_add_f32_e32 v130, v138, v139
	v_pk_mov_b32 v[144:145], v[140:141], v[142:143] op_sel:[1,0]
	v_mov_b32_e32 v141, v143
	v_pk_add_f32 v[140:141], v[144:145], v[140:141]
	v_add_f32_e32 v133, v130, v133
	v_pk_add_f32 v[140:141], v[140:141], v[140:141] op_sel:[0,1] op_sel_hi:[1,0]
	v_mov_b32_e32 v131, v132
	v_mov_b32_e32 v130, v140
	s_nop 1
	v_permlane32_swap_b32_e32 v140, v130
	v_add_f32_e32 v130, v140, v130
	v_fmamk_f32 v49, v130, 0xbc800000, v49
	v_fmamk_f32 v48, v130, 0xbc800000, v48
	v_fmamk_f32 v47, v130, 0xbc800000, v47
	v_fmamk_f32 v46, v130, 0xbc800000, v46
	v_fmamk_f32 v45, v130, 0xbc800000, v45
	v_fmamk_f32 v44, v130, 0xbc800000, v44
	v_fmamk_f32 v43, v130, 0xbc800000, v43
	v_fmamk_f32 v42, v130, 0xbc800000, v42
	v_fmamk_f32 v41, v130, 0xbc800000, v41
	v_fmamk_f32 v40, v130, 0xbc800000, v40
	v_fmamk_f32 v39, v130, 0xbc800000, v39
	v_fmamk_f32 v38, v130, 0xbc800000, v38
	v_fmamk_f32 v37, v130, 0xbc800000, v37
	v_fmamk_f32 v36, v130, 0xbc800000, v36
	v_fmamk_f32 v35, v130, 0xbc800000, v35
	v_fmac_f32_e32 v34, 0xbc800000, v130
	v_fmamk_f32 v33, v130, 0xbc800000, v33
	v_fmamk_f32 v32, v130, 0xbc800000, v32
	v_fmamk_f32 v31, v130, 0xbc800000, v31
	v_fmamk_f32 v30, v130, 0xbc800000, v30
	v_fmamk_f32 v29, v130, 0xbc800000, v29
	v_fmamk_f32 v28, v130, 0xbc800000, v28
	v_fmamk_f32 v27, v130, 0xbc800000, v27
	v_fmamk_f32 v26, v130, 0xbc800000, v26
	v_fmamk_f32 v25, v130, 0xbc800000, v25
	v_fmamk_f32 v24, v130, 0xbc800000, v24
	v_fmamk_f32 v23, v130, 0xbc800000, v23
	v_fmamk_f32 v22, v130, 0xbc800000, v22
	v_fmamk_f32 v21, v130, 0xbc800000, v21
	v_fmamk_f32 v20, v130, 0xbc800000, v20
	v_fmamk_f32 v19, v130, 0xbc800000, v19
	v_fmac_f32_e32 v18, 0xbc800000, v130
	v_pk_mul_f32 v[140:141], v[38:39], v[38:39]
	v_pk_mul_f32 v[142:143], v[46:47], v[46:47]
	v_pk_mul_f32 v[144:145], v[34:35], v[34:35]
	v_pk_mul_f32 v[146:147], v[42:43], v[42:43]
	v_pk_mul_f32 v[148:149], v[40:41], v[40:41]
	v_pk_mul_f32 v[154:155], v[48:49], v[48:49]
	v_pk_mul_f32 v[156:157], v[36:37], v[36:37]
	v_pk_mul_f32 v[158:159], v[44:45], v[44:45]
	v_pk_fma_f32 v[156:157], v[20:21], v[20:21], v[156:157]
	v_pk_fma_f32 v[158:159], v[28:29], v[28:29], v[158:159]
	v_pk_fma_f32 v[154:155], v[32:33], v[32:33], v[154:155]
	v_pk_fma_f32 v[148:149], v[24:25], v[24:25], v[148:149]
	v_pk_fma_f32 v[146:147], v[26:27], v[26:27], v[146:147]
	v_pk_fma_f32 v[144:145], v[18:19], v[18:19], v[144:145]
	v_pk_fma_f32 v[142:143], v[30:31], v[30:31], v[142:143]
	v_pk_fma_f32 v[140:141], v[22:23], v[22:23], v[140:141]
	v_permlane32_swap_b32_e32 v132, v131
	v_pk_add_f32 v[140:141], v[140:141], v[142:143]
	v_pk_add_f32 v[142:143], v[144:145], v[146:147]
	v_pk_add_f32 v[144:145], v[148:149], v[154:155]
	v_pk_add_f32 v[146:147], v[156:157], v[158:159]
	v_pk_add_f32 v[140:141], v[142:143], v[140:141]
	v_pk_add_f32 v[144:145], v[146:147], v[144:145]
	v_pk_mul_f32 v[122:123], v[122:123], v[38:39]
	v_pk_mov_b32 v[142:143], v[140:141], v[144:145] op_sel:[1,0]
	v_mov_b32_e32 v141, v145
	v_pk_add_f32 v[140:141], v[142:143], v[140:141]
	v_pk_mul_f32 v[126:127], v[126:127], v[46:47]
	v_pk_add_f32 v[140:141], v[140:141], v[140:141] op_sel:[0,1] op_sel_hi:[1,0]
	v_pk_mul_f32 v[114:115], v[114:115], v[34:35]
	v_mov_b32_e32 v130, v140
	s_nop 1
	v_permlane32_swap_b32_e32 v140, v130
	v_mov_b32_e32 v141, v132
	v_pk_add_f32 v[130:131], v[140:141], v[130:131]
	v_pk_mul_f32 v[118:119], v[118:119], v[42:43]
	v_pk_fma_f32 v[130:131], v[130:131], s[0:1], v[152:153] op_sel_hi:[1,0,0]
	v_pk_mul_f32 v[124:125], v[124:125], v[40:41]
	v_mul_f32_e32 v132, 0x4b800000, v131
	v_cmp_gt_f32_e32 vcc, s1, v131
	v_pk_mul_f32 v[128:129], v[128:129], v[48:49]
	v_pk_mul_f32 v[116:117], v[116:117], v[36:37]
	v_pk_mul_f32 v[120:121], v[120:121], v[44:45]
	v_cndmask_b32_e32 v131, v131, v132, vcc
	v_mul_f32_e32 v132, 0x4b800000, v130
	v_cmp_gt_f32_e64 s[0:1], s1, v130
	v_pk_fma_f32 v[112:113], v[112:113], v[28:29], v[120:121]
	v_pk_fma_f32 v[104:105], v[104:105], v[20:21], v[116:117]
	v_pk_fma_f32 v[108:109], v[108:109], v[32:33], v[128:129]
	v_pk_fma_f32 v[100:101], v[100:101], v[24:25], v[124:125]
	v_pk_fma_f32 v[110:111], v[110:111], v[26:27], v[118:119]
	v_pk_fma_f32 v[102:103], v[102:103], v[18:19], v[114:115]
	v_pk_fma_f32 v[106:107], v[106:107], v[30:31], v[126:127]
	v_pk_fma_f32 v[98:99], v[98:99], v[22:23], v[122:123]
	v_rsq_f32_e32 v131, v131
	v_cndmask_b32_e64 v130, v130, v132, s[0:1]
	v_pk_add_f32 v[98:99], v[98:99], v[106:107]
	v_pk_add_f32 v[102:103], v[102:103], v[110:111]
	v_pk_add_f32 v[100:101], v[100:101], v[108:109]
	v_pk_add_f32 v[104:105], v[104:105], v[112:113]
	v_rsq_f32_e32 v132, v130
	v_pk_add_f32 v[100:101], v[104:105], v[100:101]
	v_pk_add_f32 v[98:99], v[102:103], v[98:99]
	v_mul_f32_e32 v130, 0x45800000, v131
	v_add_f32_e32 v98, v98, v99
	v_add_f32_e32 v99, v100, v101
	v_add_f32_e32 v98, v98, v99
	v_mov_b32_e32 v99, v98
	v_pk_mul_f32 v[90:91], v[90:91], v[38:39]
	v_pk_mul_f32 v[94:95], v[94:95], v[46:47]
	v_pk_mul_f32 v[82:83], v[82:83], v[34:35]
	v_pk_mul_f32 v[86:87], v[86:87], v[42:43]
	v_cndmask_b32_e32 v130, v131, v130, vcc
	v_mul_f32_e32 v131, 0x45800000, v132
	v_permlane32_swap_b32_e32 v98, v99
	v_pk_fma_f32 v[78:79], v[78:79], v[26:27], v[86:87]
	v_pk_fma_f32 v[70:71], v[70:71], v[18:19], v[82:83]
	v_pk_fma_f32 v[74:75], v[74:75], v[30:31], v[94:95]
	v_pk_fma_f32 v[66:67], v[66:67], v[22:23], v[90:91]
	v_cndmask_b32_e64 v131, v132, v131, s[0:1]
	v_add_f32_e32 v98, v98, v99
	v_pk_add_f32 v[66:67], v[66:67], v[74:75]
	v_pk_add_f32 v[70:71], v[70:71], v[78:79]
	v_mul_f32_e32 v139, v160, v130
	v_mul_f32_e32 v98, v98, v131
	v_pk_add_f32 v[66:67], v[70:71], v[66:67]
	v_cmp_gt_u32_e32 vcc, 32, v1
	v_add_f32_e32 v66, v66, v67
	v_pk_mul_f32 v[92:93], v[92:93], v[40:41]
	v_cndmask_b32_e32 v67, v98, v139, vcc
	v_add_f32_e32 v67, s12, v67
	v_pk_mul_f32 v[96:97], v[96:97], v[48:49]
	v_pk_mul_f32 v[84:85], v[84:85], v[36:37]
	v_pk_mul_f32 v[88:89], v[88:89], v[44:45]
	v_mul_f32_e32 v67, 0xbfb8aa3b, v67
	v_pk_fma_f32 v[80:81], v[80:81], v[28:29], v[88:89]
	v_pk_fma_f32 v[72:73], v[72:73], v[20:21], v[84:85]
	v_pk_fma_f32 v[76:77], v[76:77], v[32:33], v[96:97]
	v_pk_fma_f32 v[68:69], v[68:69], v[24:25], v[92:93]
	v_exp_f32_e32 v70, v67
	v_pk_add_f32 v[68:69], v[68:69], v[76:77]
	v_pk_add_f32 v[72:73], v[72:73], v[80:81]
	v_cmp_lt_i32_e64 s[0:1], 0, v151
	v_pk_add_f32 v[68:69], v[72:73], v[68:69]
	v_mov_b32_e32 v137, v136
	v_add_f32_e32 v67, v68, v69
	v_add_f32_e32 v67, v66, v67
	v_add_f32_e32 v66, 1.0, v70
	v_rcp_f32_e32 v66, v66
	v_mov_b32_e32 v69, 0xff800000
	v_mov_b32_e32 v138, v133
	v_mov_b32_e32 v68, v67
	v_cndmask_b32_e64 v70, v69, v66, s[0:1]
	v_mbcnt_lo_u32_b32 v66, -1, 0
	v_mbcnt_hi_u32_b32 v66, -1, v66
	v_permlane32_swap_b32_e32 v136, v137
	v_permlane32_swap_b32_e32 v133, v138
	v_permlane32_swap_b32_e32 v67, v68
	v_and_b32_e32 v86, 64, v66
	s_mov_b32 s14, 8
	s_mov_b32 s13, 0
	v_mov_b32_e32 v66, 0
	s_waitcnt lgkmcnt(0)
